# rmsnorm1 phase: nt hint on the read-once input row loads (on top of the conv/pool phase hints)
# speedup vs baseline: 1.0162x; 1.0011x over previous
; #define LAS __attribute__((address_space(3)))
; __device__ __forceinline__ void p1_xn(const Args& a, const Frame& F) {
;     ...
;     for (int blk = F.bid; blk < 256; blk += F.G) {
;         const int mrb = blk >> 5;
;         __syncthreads();
;         for (int i = F.tid; i < 2 * 16 * 128; i += 512) { const int part = i >> 11, r = (i >> 7) & 15, c16 = i & 127;
;             *(LAS u32x4*)((part ? Wlo : Whi) + r * 2048 + ((c16 ^ r) << 4)) = *(const u32x4*)(wg + (size_t)part * 16384 + r * 1024 + c16 * 8); }
.LBB0_166:
	s_mov_b64 s[20:21], 0
	v_mov_b32_e32 v2, v152
	v_mov_b32_e32 v3, v0
	s_barrier
	v_lshrrev_b32_e32 v6, 11, v3
	v_and_b32_e32 v15, 15, v2
	v_lshlrev_b64 v[4:5], 15, v[6:7]
	v_lshlrev_b32_e32 v6, 11, v15
	v_lshl_add_u64 v[4:5], s[6:7], 0, v[4:5]
	v_lshl_add_u64 v[4:5], v[4:5], 0, v[6:7]
	v_lshl_add_u64 v[4:5], v[4:5], 0, v[12:13]
	global_load_dwordx4 v[176:179], v[4:5], off nt
	v_cmp_gt_u32_e32 vcc, s43, v3
	v_bitop3_b32 v5, v2, v146, 15 bitop3:0x6c
	v_add_u32_e32 v15, 0x200, v3
	v_cndmask_b32_e64 v4, v154, 0, vcc
	v_lshlrev_b32_e32 v5, 4, v5
	v_add_u32_e32 v2, 4, v2
	v_mov_b32_e32 v3, v15
	v_add3_u32 v208, v4, v6, v5
	v_lshrrev_b32_e32 v6, 11, v3
	v_and_b32_e32 v15, 15, v2
	v_lshlrev_b64 v[4:5], 15, v[6:7]
	v_lshlrev_b32_e32 v6, 11, v15
	v_lshl_add_u64 v[4:5], s[6:7], 0, v[4:5]
	v_lshl_add_u64 v[4:5], v[4:5], 0, v[6:7]
	v_lshl_add_u64 v[4:5], v[4:5], 0, v[12:13]
	global_load_dwordx4 v[180:183], v[4:5], off nt
	v_cmp_gt_u32_e32 vcc, s43, v3
	v_bitop3_b32 v5, v2, v146, 15 bitop3:0x6c
	v_add_u32_e32 v15, 0x200, v3
	v_cndmask_b32_e64 v4, v154, 0, vcc
	v_lshlrev_b32_e32 v5, 4, v5
	v_add_u32_e32 v2, 4, v2
	v_mov_b32_e32 v3, v15
	v_add3_u32 v209, v4, v6, v5
	v_lshrrev_b32_e32 v6, 11, v3
	v_and_b32_e32 v15, 15, v2
	v_lshlrev_b64 v[4:5], 15, v[6:7]
	v_lshlrev_b32_e32 v6, 11, v15
	v_lshl_add_u64 v[4:5], s[6:7], 0, v[4:5]
	v_lshl_add_u64 v[4:5], v[4:5], 0, v[6:7]
	v_lshl_add_u64 v[4:5], v[4:5], 0, v[12:13]
	global_load_dwordx4 v[184:187], v[4:5], off nt
	v_cmp_gt_u32_e32 vcc, s43, v3
	v_bitop3_b32 v5, v2, v146, 15 bitop3:0x6c
	v_add_u32_e32 v15, 0x200, v3
	v_cndmask_b32_e64 v4, v154, 0, vcc
	v_lshlrev_b32_e32 v5, 4, v5
	v_add_u32_e32 v2, 4, v2
	v_mov_b32_e32 v3, v15
	v_add3_u32 v210, v4, v6, v5
	v_lshrrev_b32_e32 v6, 11, v3
	v_and_b32_e32 v15, 15, v2
	v_lshlrev_b64 v[4:5], 15, v[6:7]
	v_lshlrev_b32_e32 v6, 11, v15
	v_lshl_add_u64 v[4:5], s[6:7], 0, v[4:5]
	v_lshl_add_u64 v[4:5], v[4:5], 0, v[6:7]
	v_lshl_add_u64 v[4:5], v[4:5], 0, v[12:13]
	global_load_dwordx4 v[188:191], v[4:5], off nt
	v_cmp_gt_u32_e32 vcc, s43, v3
	v_bitop3_b32 v5, v2, v146, 15 bitop3:0x6c
	v_add_u32_e32 v15, 0x200, v3
	v_cndmask_b32_e64 v4, v154, 0, vcc
	v_lshlrev_b32_e32 v5, 4, v5
	v_add_u32_e32 v2, 4, v2
	v_mov_b32_e32 v3, v15
	v_add3_u32 v211, v4, v6, v5
	v_lshrrev_b32_e32 v6, 11, v3
	v_and_b32_e32 v15, 15, v2
	v_lshlrev_b64 v[4:5], 15, v[6:7]
	v_lshlrev_b32_e32 v6, 11, v15
	v_lshl_add_u64 v[4:5], s[6:7], 0, v[4:5]
	v_lshl_add_u64 v[4:5], v[4:5], 0, v[6:7]
	v_lshl_add_u64 v[4:5], v[4:5], 0, v[12:13]
	global_load_dwordx4 v[192:195], v[4:5], off nt
	v_cmp_gt_u32_e32 vcc, s43, v3
	v_bitop3_b32 v5, v2, v146, 15 bitop3:0x6c
	v_add_u32_e32 v15, 0x200, v3
	v_cndmask_b32_e64 v4, v154, 0, vcc
	v_lshlrev_b32_e32 v5, 4, v5
	v_add_u32_e32 v2, 4, v2
	v_mov_b32_e32 v3, v15
	v_add3_u32 v212, v4, v6, v5
	v_lshrrev_b32_e32 v6, 11, v3
	v_and_b32_e32 v15, 15, v2
	v_lshlrev_b64 v[4:5], 15, v[6:7]
	v_lshlrev_b32_e32 v6, 11, v15
	v_lshl_add_u64 v[4:5], s[6:7], 0, v[4:5]
	v_lshl_add_u64 v[4:5], v[4:5], 0, v[6:7]
	v_lshl_add_u64 v[4:5], v[4:5], 0, v[12:13]
	global_load_dwordx4 v[196:199], v[4:5], off nt
	v_cmp_gt_u32_e32 vcc, s43, v3
	v_bitop3_b32 v5, v2, v146, 15 bitop3:0x6c
	v_add_u32_e32 v15, 0x200, v3
	v_cndmask_b32_e64 v4, v154, 0, vcc
	v_lshlrev_b32_e32 v5, 4, v5
	v_add_u32_e32 v2, 4, v2
	v_mov_b32_e32 v3, v15
	v_add3_u32 v213, v4, v6, v5
	v_lshrrev_b32_e32 v6, 11, v3
	v_and_b32_e32 v15, 15, v2
	v_lshlrev_b64 v[4:5], 15, v[6:7]
	v_lshlrev_b32_e32 v6, 11, v15
	v_lshl_add_u64 v[4:5], s[6:7], 0, v[4:5]
	v_lshl_add_u64 v[4:5], v[4:5], 0, v[6:7]
	v_lshl_add_u64 v[4:5], v[4:5], 0, v[12:13]
	global_load_dwordx4 v[200:203], v[4:5], off nt
	v_cmp_gt_u32_e32 vcc, s43, v3
	v_bitop3_b32 v5, v2, v146, 15 bitop3:0x6c
	v_add_u32_e32 v15, 0x200, v3
	v_cndmask_b32_e64 v4, v154, 0, vcc
	v_lshlrev_b32_e32 v5, 4, v5
	v_add_u32_e32 v2, 4, v2
	v_mov_b32_e32 v3, v15
	v_add3_u32 v214, v4, v6, v5
	v_lshrrev_b32_e32 v6, 11, v3
	v_and_b32_e32 v15, 15, v2
	v_lshlrev_b64 v[4:5], 15, v[6:7]
	v_lshlrev_b32_e32 v6, 11, v15
	v_lshl_add_u64 v[4:5], s[6:7], 0, v[4:5]
	v_lshl_add_u64 v[4:5], v[4:5], 0, v[6:7]
	v_lshl_add_u64 v[4:5], v[4:5], 0, v[12:13]
	global_load_dwordx4 v[204:207], v[4:5], off nt
	v_cmp_gt_u32_e32 vcc, s43, v3
	v_bitop3_b32 v5, v2, v146, 15 bitop3:0x6c
	v_add_u32_e32 v15, 0x200, v3
	v_cndmask_b32_e64 v4, v154, 0, vcc
	v_lshlrev_b32_e32 v5, 4, v5
	v_add_u32_e32 v2, 4, v2
	v_mov_b32_e32 v3, v15
	v_add3_u32 v215, v4, v6, v5
	s_waitcnt vmcnt(0)
; #define LAS __attribute__((address_space(3)))
; __device__ __forceinline__ void p1_xn(const Args& a, const Frame& F) {
;     ...
;             *(LAS u32x4*)((part ? Wlo : Whi) + r * 2048 + ((c16 ^ r) << 4)) = *(const u32x4*)(wg + (size_t)part * 16384 + r * 1024 + c16 * 8); }
;         for (int i = F.tid; i < 2 * 1024; i += 512) { const int mr = (i >> 10) ? 8 : mrb, k = i & 1023; NWS[i] = a.in[IN_N1W][k] * (1.0f + mod[mr * 6144 + 1024 + k]); SHV[i] = mod[mr * 6144 + k]; }
;         __syncthreads();
;         const int nstep = (blk < 32) ? 5 : 4;
	ds_write_b128 v208, v[176:179]
	ds_write_b128 v209, v[180:183]
	ds_write_b128 v210, v[184:187]
	ds_write_b128 v211, v[188:191]
	ds_write_b128 v212, v[192:195]
	ds_write_b128 v213, v[196:199]
	ds_write_b128 v214, v[200:203]
	ds_write_b128 v215, v[204:207]
	s_or_b64 exec, exec, s[20:21]
	s_lshr_b32 s20, s50, 5
	s_mul_i32 s33, s20, 0x1800
	s_mov_b64 s[20:21], 0
	v_mov_b32_e32 v2, s33
	v_mov_b32_e32 v3, v153
	v_mov_b32_e32 v4, v0
	v_cmp_gt_u32_e32 vcc, s45, v4
	v_and_b32_e32 v5, 0x3ff, v4
	v_lshlrev_b32_e32 v15, 2, v5
	v_cndmask_b32_e32 v6, v155, v2, vcc
	v_or_b32_e32 v16, v6, v5
	v_ashrrev_i32_e32 v17, 31, v16
	v_lshl_add_u64 v[16:17], v[16:17], 2, s[8:9]
	v_add_co_u32_e32 v18, vcc, 0x1000, v16
	global_load_dword v176, v15, s[48:49]
	s_nop 0
	v_addc_co_u32_e32 v19, vcc, 0, v17, vcc
	global_load_dword v180, v[18:19], off
	global_load_dword v184, v[16:17], off
	v_add_u32_e32 v4, 0x200, v4
	v_cmp_gt_u32_e32 vcc, s45, v4
	v_and_b32_e32 v5, 0x3ff, v4
	v_lshlrev_b32_e32 v15, 2, v5
	v_cndmask_b32_e32 v6, v155, v2, vcc
	v_or_b32_e32 v16, v6, v5
	v_ashrrev_i32_e32 v17, 31, v16
	v_lshl_add_u64 v[16:17], v[16:17], 2, s[8:9]
	v_add_co_u32_e32 v18, vcc, 0x1000, v16
	global_load_dword v177, v15, s[48:49]
	s_nop 0
	v_addc_co_u32_e32 v19, vcc, 0, v17, vcc
	global_load_dword v181, v[18:19], off
	global_load_dword v185, v[16:17], off
	v_add_u32_e32 v4, 0x200, v4
	v_cmp_gt_u32_e32 vcc, s45, v4
	v_and_b32_e32 v5, 0x3ff, v4
	v_lshlrev_b32_e32 v15, 2, v5
	v_cndmask_b32_e32 v6, v155, v2, vcc
	v_or_b32_e32 v16, v6, v5
	v_ashrrev_i32_e32 v17, 31, v16
	v_lshl_add_u64 v[16:17], v[16:17], 2, s[8:9]
	v_add_co_u32_e32 v18, vcc, 0x1000, v16
	global_load_dword v178, v15, s[48:49]
	s_nop 0
	v_addc_co_u32_e32 v19, vcc, 0, v17, vcc
	global_load_dword v182, v[18:19], off
	global_load_dword v186, v[16:17], off
	v_add_u32_e32 v4, 0x200, v4
	v_cmp_gt_u32_e32 vcc, s45, v4
	v_and_b32_e32 v5, 0x3ff, v4
	v_lshlrev_b32_e32 v15, 2, v5
	v_cndmask_b32_e32 v6, v155, v2, vcc
	v_or_b32_e32 v16, v6, v5
	v_ashrrev_i32_e32 v17, 31, v16
	v_lshl_add_u64 v[16:17], v[16:17], 2, s[8:9]
	v_add_co_u32_e32 v18, vcc, 0x1000, v16
	global_load_dword v179, v15, s[48:49]
	s_nop 0
	v_addc_co_u32_e32 v19, vcc, 0, v17, vcc
	global_load_dword v183, v[18:19], off
	global_load_dword v187, v[16:17], off
	v_add_u32_e32 v4, 0x200, v4
	v_add_u32_e32 v16, 0xffffe000, v3
	s_waitcnt vmcnt(0)
	v_add_f32_e32 v6, 1.0, v180
	ds_write_b32 v3, v184
	v_mul_f32_e32 v5, v176, v6
	ds_write_b32 v16, v5
	v_add_f32_e32 v6, 1.0, v181
	ds_write_b32 v3, v185 offset:2048
	v_mul_f32_e32 v5, v177, v6
	ds_write_b32 v16, v5 offset:2048
	v_add_f32_e32 v6, 1.0, v182
	ds_write_b32 v3, v186 offset:4096
	v_mul_f32_e32 v5, v178, v6
	ds_write_b32 v16, v5 offset:4096
	v_add_f32_e32 v6, 1.0, v183
	ds_write_b32 v3, v187 offset:6144
	v_mul_f32_e32 v5, v179, v6
	ds_write_b32 v16, v5 offset:6144
	s_or_b64 exec, exec, s[20:21]
	s_cmp_lt_i32 s50, 32
	s_cselect_b32 s51, 20, 16
	s_lshl_b32 s58, s50, 2
	s_addk_i32 s58, 0x1000
	s_mov_b32 s59, 0
	s_waitcnt lgkmcnt(0)
	s_barrier
	s_branch .LBB0_172

; template <int NT, bool XBF16> ...
;     ...
;     } else {
;         const int lnx = c + 16 * q, iaddr = 4 * (4 * c + q);
;         const f32x4* xp = (const f32x4*)xrow + 128 * hf + 2 * (lnx & 3);
; #pragma unroll
;         for (int j = 0; j < 16; ++j) { xa[j] = xp[j * 8]; xb[j] = xp[j * 8 + 1]; }
; #pragma unroll
;         for (int j = 0; j < 16; ++j) { xa[j] = __builtin_bit_cast(f32x4, lane_perm(__builtin_bit_cast(u32x4, xa[j]), iaddr)); xb[j] = __builtin_bit_cast(f32x4, lane_perm(__builtin_bit_cast(u32x4, xb[j]), iaddr)); }
;     }
;     float ss = 0.f;
; #pragma unroll
;     for (int j = 0; j < 16; ++j) ss += ((xa[j].x * xa[j].x + xa[j].y * xa[j].y) + (xa[j].z * xa[j].z + xa[j].w * xa[j].w)) + ((xb[j].x * xb[j].x + xb[j].y * xb[j].y) + (xb[j].z * xb[j].z + xb[j].w * xb[j].w));
.LBB0_176:
	v_lshl_add_u64 v[2:3], v[2:3], 0, s[10:11]
	v_mov_b32_e32 v15, v7
	v_lshl_add_u64 v[78:79], v[2:3], 0, v[14:15]
	global_load_dwordx4 v[2:5], v[78:79], off nt
	global_load_dwordx4 v[16:19], v[78:79], off offset:16 nt
	global_load_dwordx4 v[20:23], v[78:79], off offset:128 nt
	global_load_dwordx4 v[24:27], v[78:79], off offset:144 nt
	global_load_dwordx4 v[28:31], v[78:79], off offset:256 nt
	global_load_dwordx4 v[32:35], v[78:79], off offset:272 nt
	global_load_dwordx4 v[36:39], v[78:79], off offset:384 nt
	global_load_dwordx4 v[40:43], v[78:79], off offset:400 nt
	global_load_dwordx4 v[44:47], v[78:79], off offset:512 nt
	global_load_dwordx4 v[50:53], v[78:79], off offset:528 nt
	global_load_dwordx4 v[54:57], v[78:79], off offset:640 nt
	global_load_dwordx4 v[58:61], v[78:79], off offset:656 nt
	global_load_dwordx4 v[62:65], v[78:79], off offset:768 nt
	global_load_dwordx4 v[66:69], v[78:79], off offset:784 nt
	global_load_dwordx4 v[70:73], v[78:79], off offset:896 nt
	global_load_dwordx4 v[74:77], v[78:79], off offset:912 nt
	global_load_dwordx4 v[174:177], v[78:79], off offset:1024 nt
	global_load_dwordx4 v[178:181], v[78:79], off offset:1040 nt
	global_load_dwordx4 v[182:185], v[78:79], off offset:1168 nt
	global_load_dwordx4 v[186:189], v[78:79], off offset:1152 nt
	global_load_dwordx4 v[190:193], v[78:79], off offset:1296 nt
	global_load_dwordx4 v[194:197], v[78:79], off offset:1280 nt
	global_load_dwordx4 v[200:203], v[78:79], off offset:1424 nt
	global_load_dwordx4 v[204:207], v[78:79], off offset:1408 nt
	global_load_dwordx4 v[208:211], v[78:79], off offset:1552 nt
	global_load_dwordx4 v[212:215], v[78:79], off offset:1536 nt
	global_load_dwordx4 v[216:219], v[78:79], off offset:1664 nt
	global_load_dwordx4 v[220:223], v[78:79], off offset:1680 nt
	global_load_dwordx4 v[224:227], v[78:79], off offset:1792 nt
	global_load_dwordx4 v[228:231], v[78:79], off offset:1808 nt
	global_load_dwordx4 v[232:235], v[78:79], off offset:1920 nt
	global_load_dwordx4 v[236:239], v[78:79], off offset:1936 nt
	s_waitcnt vmcnt(31)
	ds_bpermute_b32 v139, v142, v3
	ds_bpermute_b32 v141, v142, v5
	ds_bpermute_b32 v138, v142, v2
	ds_bpermute_b32 v140, v142, v4
	s_waitcnt vmcnt(30)
	ds_bpermute_b32 v137, v142, v17
	ds_bpermute_b32 v135, v142, v19
	ds_bpermute_b32 v136, v142, v16
	ds_bpermute_b32 v134, v142, v18
	s_waitcnt vmcnt(29)
	ds_bpermute_b32 v131, v142, v21
	ds_bpermute_b32 v133, v142, v23
	s_waitcnt lgkmcnt(9)
	v_mul_f32_e32 v6, v139, v139
	s_waitcnt lgkmcnt(8)
	v_mul_f32_e32 v15, v141, v141
	ds_bpermute_b32 v130, v142, v20
	ds_bpermute_b32 v132, v142, v22
	s_waitcnt lgkmcnt(9)
	v_fmac_f32_e32 v6, v138, v138
	s_waitcnt lgkmcnt(8)
	v_fmac_f32_e32 v15, v140, v140
	s_waitcnt vmcnt(28)
	ds_bpermute_b32 v129, v142, v25
	ds_bpermute_b32 v127, v142, v27
	s_waitcnt vmcnt(16)
	ds_bpermute_b32 v80, v142, v74
	s_waitcnt vmcnt(15)
	ds_bpermute_b32 v74, v142, v174
	v_add_f32_e32 v6, v6, v15
	s_waitcnt lgkmcnt(11)
	v_mul_f32_e32 v15, v137, v137
	s_waitcnt lgkmcnt(10)
	v_mul_f32_e32 v174, v135, v135
	ds_bpermute_b32 v128, v142, v24
	ds_bpermute_b32 v126, v142, v26
	s_waitcnt lgkmcnt(11)
	v_fmac_f32_e32 v15, v136, v136
	s_waitcnt lgkmcnt(10)
	v_fmac_f32_e32 v174, v134, v134
	v_add_f32_e32 v15, v15, v174
	v_add_f32_e32 v6, v6, v15
	s_waitcnt lgkmcnt(9)
	v_mul_f32_e32 v15, v131, v131
	s_waitcnt lgkmcnt(8)
	v_mul_f32_e32 v174, v133, v133
	ds_bpermute_b32 v123, v142, v29
	ds_bpermute_b32 v125, v142, v31
	s_waitcnt lgkmcnt(9)
	v_fmac_f32_e32 v15, v130, v130
	s_waitcnt lgkmcnt(8)
	v_fmac_f32_e32 v174, v132, v132
	ds_bpermute_b32 v122, v142, v28
	ds_bpermute_b32 v124, v142, v30
	ds_bpermute_b32 v81, v142, v75
	ds_bpermute_b32 v75, v142, v175
	v_add_f32_e32 v15, v15, v174
	s_waitcnt lgkmcnt(11)
	v_mul_f32_e32 v174, v129, v129
	s_waitcnt lgkmcnt(10)
	v_mul_f32_e32 v175, v127, v127
	ds_bpermute_b32 v121, v142, v33
	ds_bpermute_b32 v119, v142, v35
	s_waitcnt lgkmcnt(9)
	v_fmac_f32_e32 v174, v128, v128
	s_waitcnt lgkmcnt(8)
	v_fmac_f32_e32 v175, v126, v126
	ds_bpermute_b32 v120, v142, v32
	ds_bpermute_b32 v118, v142, v34
	v_add_f32_e32 v174, v174, v175
	v_add_f32_e32 v15, v15, v174
	v_add_f32_e32 v6, v6, v15
	s_waitcnt lgkmcnt(9)
	v_mul_f32_e32 v15, v123, v123
	s_waitcnt lgkmcnt(8)
	v_mul_f32_e32 v174, v125, v125
	ds_bpermute_b32 v115, v142, v37
	ds_bpermute_b32 v117, v142, v39
	s_waitcnt lgkmcnt(9)
	v_fmac_f32_e32 v15, v122, v122
	s_waitcnt lgkmcnt(8)
	v_fmac_f32_e32 v174, v124, v124
	ds_bpermute_b32 v114, v142, v36
	ds_bpermute_b32 v116, v142, v38
	v_add_f32_e32 v15, v15, v174
	s_waitcnt lgkmcnt(7)
	v_mul_f32_e32 v174, v121, v121
	s_waitcnt lgkmcnt(6)
	v_mul_f32_e32 v175, v119, v119
	ds_bpermute_b32 v113, v142, v41
	ds_bpermute_b32 v111, v142, v43
	s_waitcnt lgkmcnt(7)
	v_fmac_f32_e32 v174, v120, v120
	s_waitcnt lgkmcnt(6)
	v_fmac_f32_e32 v175, v118, v118
	ds_bpermute_b32 v112, v142, v40
	ds_bpermute_b32 v110, v142, v42
	v_add_f32_e32 v174, v174, v175
	v_add_f32_e32 v15, v15, v174
	v_add_f32_e32 v6, v6, v15
	s_waitcnt lgkmcnt(7)
	v_mul_f32_e32 v15, v115, v115
	s_waitcnt lgkmcnt(6)
	v_mul_f32_e32 v174, v117, v117
	ds_bpermute_b32 v107, v142, v45
	ds_bpermute_b32 v109, v142, v47
	s_waitcnt lgkmcnt(7)
	v_fmac_f32_e32 v15, v114, v114
	s_waitcnt lgkmcnt(6)
	v_fmac_f32_e32 v174, v116, v116
	ds_bpermute_b32 v106, v142, v44
	ds_bpermute_b32 v108, v142, v46
	v_add_f32_e32 v15, v15, v174
	s_waitcnt lgkmcnt(7)
	v_mul_f32_e32 v174, v113, v113
	s_waitcnt lgkmcnt(6)
	v_mul_f32_e32 v175, v111, v111
	ds_bpermute_b32 v105, v142, v51
	ds_bpermute_b32 v103, v142, v53
	s_waitcnt lgkmcnt(7)
	v_fmac_f32_e32 v174, v112, v112
	s_waitcnt lgkmcnt(6)
; template <int NT, bool XBF16> ...
;     ...
;         for (int j = 0; j < 16; ++j) { xa[j] = __builtin_bit_cast(f32x4, lane_perm(__builtin_bit_cast(u32x4, xa[j]), iaddr)); xb[j] = __builtin_bit_cast(f32x4, lane_perm(__builtin_bit_cast(u32x4, xb[j]), iaddr)); }
;     }
;     float ss = 0.f;
; #pragma unroll
;     for (int j = 0; j < 16; ++j) ss += ((xa[j].x * xa[j].x + xa[j].y * xa[j].y) + (xa[j].z * xa[j].z + xa[j].w * xa[j].w)) + ((xb[j].x * xb[j].x + xb[j].y * xb[j].y) + (xb[j].z * xb[j].z + xb[j].w * xb[j].w));
	v_fmac_f32_e32 v175, v110, v110
	ds_bpermute_b32 v104, v142, v50
	ds_bpermute_b32 v102, v142, v52
	v_add_f32_e32 v174, v174, v175
	v_add_f32_e32 v15, v15, v174
	v_add_f32_e32 v6, v6, v15
	s_waitcnt lgkmcnt(7)
	v_mul_f32_e32 v15, v107, v107
	s_waitcnt lgkmcnt(6)
	v_mul_f32_e32 v174, v109, v109
	ds_bpermute_b32 v99, v142, v55
	ds_bpermute_b32 v101, v142, v57
	s_waitcnt lgkmcnt(7)
	v_fmac_f32_e32 v15, v106, v106
	s_waitcnt lgkmcnt(6)
	v_fmac_f32_e32 v174, v108, v108
	ds_bpermute_b32 v98, v142, v54
	ds_bpermute_b32 v100, v142, v56
	v_add_f32_e32 v15, v15, v174
	s_waitcnt lgkmcnt(7)
	v_mul_f32_e32 v174, v105, v105
	s_waitcnt lgkmcnt(6)
	v_mul_f32_e32 v175, v103, v103
	ds_bpermute_b32 v97, v142, v59
	ds_bpermute_b32 v95, v142, v61
	s_waitcnt lgkmcnt(7)
	v_fmac_f32_e32 v174, v104, v104
	s_waitcnt lgkmcnt(6)
	v_fmac_f32_e32 v175, v102, v102
	ds_bpermute_b32 v96, v142, v58
	ds_bpermute_b32 v94, v142, v60
	v_add_f32_e32 v174, v174, v175
	v_add_f32_e32 v15, v15, v174
	v_add_f32_e32 v6, v6, v15
	s_waitcnt lgkmcnt(7)
	v_mul_f32_e32 v15, v99, v99
	s_waitcnt lgkmcnt(6)
	v_mul_f32_e32 v174, v101, v101
	ds_bpermute_b32 v91, v142, v63
	ds_bpermute_b32 v93, v142, v65
	s_waitcnt lgkmcnt(7)
	v_fmac_f32_e32 v15, v98, v98
	s_waitcnt lgkmcnt(6)
	v_fmac_f32_e32 v174, v100, v100
	ds_bpermute_b32 v90, v142, v62
	ds_bpermute_b32 v92, v142, v64
	v_add_f32_e32 v15, v15, v174
	s_waitcnt lgkmcnt(7)
	v_mul_f32_e32 v174, v97, v97
	s_waitcnt lgkmcnt(6)
	v_mul_f32_e32 v175, v95, v95
	ds_bpermute_b32 v89, v142, v67
	ds_bpermute_b32 v87, v142, v69
	s_waitcnt lgkmcnt(7)
	v_fmac_f32_e32 v174, v96, v96
	s_waitcnt lgkmcnt(6)
	v_fmac_f32_e32 v175, v94, v94
	ds_bpermute_b32 v88, v142, v66
	ds_bpermute_b32 v86, v142, v68
	v_add_f32_e32 v174, v174, v175
	v_add_f32_e32 v15, v15, v174
	v_add_f32_e32 v6, v6, v15
	s_waitcnt lgkmcnt(7)
	v_mul_f32_e32 v15, v91, v91
	s_waitcnt lgkmcnt(6)
	v_mul_f32_e32 v174, v93, v93
	ds_bpermute_b32 v83, v142, v71
	ds_bpermute_b32 v85, v142, v73
	s_waitcnt lgkmcnt(7)
	v_fmac_f32_e32 v15, v90, v90
	s_waitcnt lgkmcnt(6)
	v_fmac_f32_e32 v174, v92, v92
	ds_bpermute_b32 v82, v142, v70
	ds_bpermute_b32 v84, v142, v72
	v_add_f32_e32 v15, v15, v174
	s_waitcnt lgkmcnt(7)
	v_mul_f32_e32 v174, v89, v89
	s_waitcnt lgkmcnt(6)
	v_mul_f32_e32 v175, v87, v87
	ds_bpermute_b32 v79, v142, v77
	s_waitcnt lgkmcnt(6)
	v_fmac_f32_e32 v174, v88, v88
	s_waitcnt lgkmcnt(5)
	v_fmac_f32_e32 v175, v86, v86
	ds_bpermute_b32 v78, v142, v76
	v_add_f32_e32 v174, v174, v175
	v_add_f32_e32 v15, v15, v174
	v_add_f32_e32 v6, v6, v15
	s_waitcnt lgkmcnt(5)
	v_mul_f32_e32 v15, v83, v83
	s_waitcnt lgkmcnt(4)
	v_mul_f32_e32 v174, v85, v85
	ds_bpermute_b32 v77, v142, v177
	s_waitcnt lgkmcnt(4)
	v_fmac_f32_e32 v15, v82, v82
	s_waitcnt lgkmcnt(3)
	v_fmac_f32_e32 v174, v84, v84
	ds_bpermute_b32 v76, v142, v176
	v_add_f32_e32 v15, v15, v174
	v_mul_f32_e32 v174, v81, v81
	s_waitcnt lgkmcnt(3)
	v_mul_f32_e32 v175, v79, v79
	s_waitcnt vmcnt(14)
	ds_bpermute_b32 v73, v142, v179
	ds_bpermute_b32 v71, v142, v181
	v_fmac_f32_e32 v174, v80, v80
	s_waitcnt lgkmcnt(4)
	v_fmac_f32_e32 v175, v78, v78
	ds_bpermute_b32 v72, v142, v178
	ds_bpermute_b32 v70, v142, v180
	v_add_f32_e32 v174, v174, v175
	v_add_f32_e32 v15, v15, v174
	v_add_f32_e32 v6, v6, v15
	v_mul_f32_e32 v15, v75, v75
	s_waitcnt lgkmcnt(5)
	v_mul_f32_e32 v174, v77, v77
	s_waitcnt vmcnt(12)
	ds_bpermute_b32 v67, v142, v187
	ds_bpermute_b32 v69, v142, v189
	v_fmac_f32_e32 v15, v74, v74
	s_waitcnt lgkmcnt(6)
	v_fmac_f32_e32 v174, v76, v76
	ds_bpermute_b32 v66, v142, v186
	ds_bpermute_b32 v68, v142, v188
	v_add_f32_e32 v15, v15, v174
	s_waitcnt lgkmcnt(7)
	v_mul_f32_e32 v174, v73, v73
	s_waitcnt lgkmcnt(6)
	v_mul_f32_e32 v175, v71, v71
	ds_bpermute_b32 v65, v142, v183
	ds_bpermute_b32 v63, v142, v185
	s_waitcnt lgkmcnt(7)
	v_fmac_f32_e32 v174, v72, v72
	s_waitcnt lgkmcnt(6)
	v_fmac_f32_e32 v175, v70, v70
	ds_bpermute_b32 v64, v142, v182
	ds_bpermute_b32 v62, v142, v184
	v_add_f32_e32 v174, v174, v175
	v_add_f32_e32 v15, v15, v174
	v_add_f32_e32 v6, v6, v15
	s_waitcnt lgkmcnt(7)
	v_mul_f32_e32 v15, v67, v67
	s_waitcnt lgkmcnt(6)
	v_mul_f32_e32 v174, v69, v69
	s_waitcnt vmcnt(10)
	ds_bpermute_b32 v59, v142, v195
	ds_bpermute_b32 v61, v142, v197
	s_waitcnt lgkmcnt(7)
	v_fmac_f32_e32 v15, v66, v66
	s_waitcnt lgkmcnt(6)
	v_fmac_f32_e32 v174, v68, v68
	ds_bpermute_b32 v58, v142, v194
	ds_bpermute_b32 v60, v142, v196
	v_add_f32_e32 v15, v15, v174
	s_waitcnt lgkmcnt(7)
	v_mul_f32_e32 v174, v65, v65
	s_waitcnt lgkmcnt(6)
	v_mul_f32_e32 v175, v63, v63
	ds_bpermute_b32 v57, v142, v191
	ds_bpermute_b32 v55, v142, v193
	s_waitcnt lgkmcnt(7)
	v_fmac_f32_e32 v174, v64, v64
	s_waitcnt lgkmcnt(6)
	v_fmac_f32_e32 v175, v62, v62
	ds_bpermute_b32 v56, v142, v190
	ds_bpermute_b32 v54, v142, v192
	v_add_f32_e32 v174, v174, v175
	v_add_f32_e32 v15, v15, v174
	v_add_f32_e32 v6, v6, v15
	s_waitcnt lgkmcnt(7)
	v_mul_f32_e32 v15, v59, v59
	s_waitcnt lgkmcnt(6)
; template <int NT, bool XBF16> ...
;     ...
;         for (int j = 0; j < 16; ++j) { xa[j] = __builtin_bit_cast(f32x4, lane_perm(__builtin_bit_cast(u32x4, xa[j]), iaddr)); xb[j] = __builtin_bit_cast(f32x4, lane_perm(__builtin_bit_cast(u32x4, xb[j]), iaddr)); }
;     }
;     float ss = 0.f;
; #pragma unroll
;     for (int j = 0; j < 16; ++j) ss += ((xa[j].x * xa[j].x + xa[j].y * xa[j].y) + (xa[j].z * xa[j].z + xa[j].w * xa[j].w)) + ((xb[j].x * xb[j].x + xb[j].y * xb[j].y) + (xb[j].z * xb[j].z + xb[j].w * xb[j].w));
;     ss += __shfl_xor(ss, 16); ss += __shfl_xor(ss, 32);
;     if (q == 0) red[wave * 16 + c] = ss;
	v_mul_f32_e32 v174, v61, v61
	s_waitcnt vmcnt(8)
	ds_bpermute_b32 v51, v142, v205
	ds_bpermute_b32 v53, v142, v207
	s_waitcnt lgkmcnt(7)
	v_fmac_f32_e32 v15, v58, v58
	s_waitcnt lgkmcnt(6)
	v_fmac_f32_e32 v174, v60, v60
	ds_bpermute_b32 v50, v142, v204
	ds_bpermute_b32 v52, v142, v206
	v_add_f32_e32 v15, v15, v174
	s_waitcnt lgkmcnt(7)
	v_mul_f32_e32 v174, v57, v57
	s_waitcnt lgkmcnt(6)
	v_mul_f32_e32 v175, v55, v55
	ds_bpermute_b32 v47, v142, v201
	ds_bpermute_b32 v45, v142, v203
	s_waitcnt lgkmcnt(7)
	v_fmac_f32_e32 v174, v56, v56
	s_waitcnt lgkmcnt(6)
	v_fmac_f32_e32 v175, v54, v54
	ds_bpermute_b32 v46, v142, v200
	ds_bpermute_b32 v44, v142, v202
	v_add_f32_e32 v174, v174, v175
	v_add_f32_e32 v15, v15, v174
	v_add_f32_e32 v6, v6, v15
	s_waitcnt lgkmcnt(7)
	v_mul_f32_e32 v15, v51, v51
	s_waitcnt lgkmcnt(6)
	v_mul_f32_e32 v174, v53, v53
	s_waitcnt vmcnt(6)
	ds_bpermute_b32 v41, v142, v213
	ds_bpermute_b32 v43, v142, v215
	s_waitcnt lgkmcnt(7)
	v_fmac_f32_e32 v15, v50, v50
	s_waitcnt lgkmcnt(6)
	v_fmac_f32_e32 v174, v52, v52
	ds_bpermute_b32 v40, v142, v212
	ds_bpermute_b32 v42, v142, v214
	v_add_f32_e32 v15, v15, v174
	s_waitcnt lgkmcnt(7)
	v_mul_f32_e32 v174, v47, v47
	s_waitcnt lgkmcnt(6)
	v_mul_f32_e32 v175, v45, v45
	ds_bpermute_b32 v39, v142, v209
	ds_bpermute_b32 v37, v142, v211
	s_waitcnt lgkmcnt(7)
	v_fmac_f32_e32 v174, v46, v46
	s_waitcnt lgkmcnt(6)
	v_fmac_f32_e32 v175, v44, v44
	ds_bpermute_b32 v38, v142, v208
	ds_bpermute_b32 v36, v142, v210
	v_add_f32_e32 v174, v174, v175
	v_add_f32_e32 v15, v15, v174
	v_add_f32_e32 v6, v6, v15
	s_waitcnt lgkmcnt(7)
	v_mul_f32_e32 v15, v41, v41
	s_waitcnt lgkmcnt(6)
	v_mul_f32_e32 v174, v43, v43
	s_waitcnt vmcnt(5)
	ds_bpermute_b32 v33, v142, v217
	ds_bpermute_b32 v35, v142, v219
	s_waitcnt lgkmcnt(7)
	v_fmac_f32_e32 v15, v40, v40
	s_waitcnt lgkmcnt(6)
	v_fmac_f32_e32 v174, v42, v42
	ds_bpermute_b32 v32, v142, v216
	ds_bpermute_b32 v34, v142, v218
	v_add_f32_e32 v15, v15, v174
	s_waitcnt lgkmcnt(7)
	v_mul_f32_e32 v174, v39, v39
	s_waitcnt lgkmcnt(6)
	v_mul_f32_e32 v175, v37, v37
	s_waitcnt vmcnt(4)
	ds_bpermute_b32 v31, v142, v221
	ds_bpermute_b32 v29, v142, v223
	s_waitcnt lgkmcnt(7)
	v_fmac_f32_e32 v174, v38, v38
	s_waitcnt lgkmcnt(6)
	v_fmac_f32_e32 v175, v36, v36
	ds_bpermute_b32 v30, v142, v220
	ds_bpermute_b32 v28, v142, v222
	v_add_f32_e32 v174, v174, v175
	v_add_f32_e32 v15, v15, v174
	v_add_f32_e32 v6, v6, v15
	s_waitcnt lgkmcnt(7)
	v_mul_f32_e32 v15, v33, v33
	s_waitcnt lgkmcnt(6)
	v_mul_f32_e32 v174, v35, v35
	s_waitcnt vmcnt(3)
	ds_bpermute_b32 v25, v142, v225
	ds_bpermute_b32 v27, v142, v227
	s_waitcnt lgkmcnt(7)
	v_fmac_f32_e32 v15, v32, v32
	s_waitcnt lgkmcnt(6)
	v_fmac_f32_e32 v174, v34, v34
	ds_bpermute_b32 v24, v142, v224
	ds_bpermute_b32 v26, v142, v226
	v_add_f32_e32 v15, v15, v174
	s_waitcnt lgkmcnt(7)
	v_mul_f32_e32 v174, v31, v31
	s_waitcnt lgkmcnt(6)
	v_mul_f32_e32 v175, v29, v29
	s_waitcnt vmcnt(2)
	ds_bpermute_b32 v23, v142, v229
	ds_bpermute_b32 v21, v142, v231
	s_waitcnt lgkmcnt(7)
	v_fmac_f32_e32 v174, v30, v30
	s_waitcnt lgkmcnt(6)
	v_fmac_f32_e32 v175, v28, v28
	ds_bpermute_b32 v22, v142, v228
	ds_bpermute_b32 v20, v142, v230
	v_add_f32_e32 v174, v174, v175
	v_add_f32_e32 v15, v15, v174
	v_add_f32_e32 v6, v6, v15
	s_waitcnt lgkmcnt(7)
	v_mul_f32_e32 v15, v25, v25
	s_waitcnt lgkmcnt(6)
	v_mul_f32_e32 v174, v27, v27
	s_waitcnt vmcnt(1)
	ds_bpermute_b32 v17, v142, v233
	ds_bpermute_b32 v19, v142, v235
	s_waitcnt lgkmcnt(7)
	v_fmac_f32_e32 v15, v24, v24
	s_waitcnt lgkmcnt(6)
	v_fmac_f32_e32 v174, v26, v26
	ds_bpermute_b32 v16, v142, v232
	ds_bpermute_b32 v18, v142, v234
	v_add_f32_e32 v15, v15, v174
	s_waitcnt lgkmcnt(7)
	v_mul_f32_e32 v174, v23, v23
	s_waitcnt lgkmcnt(6)
	v_mul_f32_e32 v175, v21, v21
	s_waitcnt vmcnt(0)
	ds_bpermute_b32 v5, v142, v237
	ds_bpermute_b32 v3, v142, v239
	s_waitcnt lgkmcnt(7)
	v_fmac_f32_e32 v174, v22, v22
	s_waitcnt lgkmcnt(6)
	v_fmac_f32_e32 v175, v20, v20
	ds_bpermute_b32 v4, v142, v236
	ds_bpermute_b32 v2, v142, v238
	v_add_f32_e32 v174, v174, v175
	v_add_f32_e32 v15, v15, v174
	v_add_f32_e32 v6, v6, v15
	s_waitcnt lgkmcnt(7)
	v_mul_f32_e32 v15, v17, v17
	s_waitcnt lgkmcnt(6)
	v_mul_f32_e32 v174, v19, v19
	s_waitcnt lgkmcnt(5)
	v_fmac_f32_e32 v15, v16, v16
	s_waitcnt lgkmcnt(4)
	v_fmac_f32_e32 v174, v18, v18
	v_add_f32_e32 v15, v15, v174
	s_waitcnt lgkmcnt(3)
	v_mul_f32_e32 v174, v5, v5
	s_waitcnt lgkmcnt(2)
	v_mul_f32_e32 v175, v3, v3
	s_waitcnt lgkmcnt(1)
	v_fmac_f32_e32 v174, v4, v4
	s_waitcnt lgkmcnt(0)
	v_fmac_f32_e32 v175, v2, v2
	v_add_f32_e32 v174, v174, v175
	v_add_f32_e32 v15, v15, v174
	v_add_f32_e32 v6, v6, v15
	ds_bpermute_b32 v15, v143, v6
	s_waitcnt lgkmcnt(0)
	v_add_f32_e32 v6, v6, v15
	ds_bpermute_b32 v15, v144, v6
	s_and_saveexec_b64 s[20:21], s[0:1]
	s_cbranch_execz .LBB0_178
	s_waitcnt lgkmcnt(0)
	v_add_f32_e32 v6, v6, v15
	ds_write_b32 v173, v6
